# hosted conversion pipelined (counted waits allow next tile's loads in flight, only on P6-idle CUs); P4 converts items [0,22848), P6-idle CUs [22848,39168)
# baseline (speedup 1.0000x reference)
; #define LAS __attribute__((address_space(3)))
; #define LAS __attribute__((address_space(3)))
;     LAS unsigned* scr = (LAS unsigned*)(lds + wave * 16384);
;     WItem d0, d1; WRegs R0, R1;
;     constexpr int KB_ = DM / 32;
;     constexpr int NALL = EARLY ? KB_ * (INW / 128) : KB_ * (DM / 128) + KB_ * (CW / 128) + KB_ * (2 * CW / 128) + (CW / 32) * (DM / 128) + KB_ * (DFF2 / 128) + (DFF / 32) * (DM / 128);
;     const int hi_all = it_hi < NALL ? it_hi : NALL, total = hi_all - it_lo, nwgs = NGW / NWAVES, chunk = (((total + nwgs - 1) / nwgs) + NWAVES - 1) / NWAVES * NWAVES;
;     int it = it_lo + (gw / NWAVES) * chunk + (gw % NWAVES); const int wend0 = it_lo + (gw / NWAVES + 1) * chunk, wend = wend0 < hi_all ? wend0 : hi_all;
; __global__ void __launch_bounds__(NWAVES * 64, 2) mk_fwd(Args args) {
;     ...
;         const int NCONV = (CONV_OVERLAP && G >= 128) ? 51 : 0;
;         if (bx < NCONV) convert_weights<false, true>(P, lds, bx * NWAVES + wave, NCONV * NWAVES, wave, lane, 0, (CONV_OVERLAP && G >= 192) ? LATE_SPLIT : 0x7fffffff);
;         else {
;             sb_phase(lds, PROJ, (bf16*)(ws + WS_MIX), (const float*)(ws + WS_RSB), P.sbo_norm, bx - NCONV, G - NCONV, tid);
;             ret_out_phase(lds, PROJ, (bf16*)(ws + WS_MIX), (const bf16*)(ws + WS_ST), P.ret_norm, bx - NCONV, G - NCONV, tid);
;         }
;         if (NCONV == 0) convert_weights<false>(P, lds, gw, NGW, wave, lane);
.LBB0_519:
	s_mov_b32 s98, 0
	s_mov_b32 s99, 0
	s_mov_b32 s100, s80
	s_mov_b32 s101, s56
	s_mov_b32 s0, 0x9900
	s_cmp_eq_u32 s80, 0x100
	s_cselect_b32 s1, 1, 0
	s_cmp_gt_i32 s75, 6
	s_cselect_b32 s1, s1, 0
	s_cmp_lg_u32 s1, 0
	s_cselect_b32 s0, 0x5940, s0
	v_writelane_b32 v255, s0, 2
	s_mov_b32 s0, 0
	v_writelane_b32 v255, s0, 3

; #define GAS __attribute__((address_space(1)))
; template <bool UNCOND> DI void witem_load(const WItem& d, WRegs& R, int lane) {
;     const int n4 = lane & 31, kh = lane >> 5;
;     const float* src = d.W + (size_t)(d.k0 + 2 * kh) * d.N + d.src_col0 + 4 * n4;
; #pragma unroll
;     for (int i = 0; i < 8; ++i) { R.a[i] = *(const GAS f32x4*)(src + (size_t)(4 * i) * d.N); R.b[i] = *(const GAS f32x4*)(src + (size_t)(4 * i + 1) * d.N); }
;     if (UNCOND) {
;         const float* gp = d.gain ? d.gain + d.k0 + 2 * kh : src;
; #pragma unroll
;         for (int i = 0; i < 8; ++i) R.gg[i] = *(const GAS f32x2g*)(gp + 4 * i);
;         if (!d.gain) {
; #pragma unroll
;             for (int i = 0; i < 8; ++i) R.gg[i] = (f32x2g){1.f, 1.f}; }
;     } else if (d.gain) {
; #pragma unroll
;         for (int i = 0; i < 8; ++i) R.gg[i] = *(const GAS f32x2g*)(d.gain + d.k0 + 4 * i + 2 * kh); }
;     else {
; #pragma unroll
;         for (int i = 0; i < 8; ++i) R.gg[i] = (f32x2g){1.f, 1.f}; }
; }
.LBB0_611:
	v_cndmask_b32_e64 v150, 0, 1, s[4:5]
	v_cmp_ne_u32_e64 s[0:1], 1, v150
	s_andn2_b64 vcc, exec, s[4:5]
	s_mov_b32 s100, 0
	s_cbranch_vccnz .LBB0_615
	v_add_u32_e32 v66, s36, v146
	v_mad_i64_i32 v[66:67], s[4:5], s38, v66, 0
	v_lshl_add_u64 v[66:67], v[66:67], 2, s[30:31]
	s_ashr_i32 s43, s42, 31
	s_ashr_i32 s39, s38, 31
	v_lshl_add_u64 v[66:67], s[42:43], 2, v[66:67]
	v_lshlrev_b32_e32 v150, 2, v148
	v_lshl_add_u64 v[66:67], v[66:67], 0, v[150:151]
	s_lshl_b64 s[4:5], s[38:39], 2
	v_lshl_add_u64 v[70:71], v[66:67], 0, s[4:5]
	global_load_dwordx4 v[66:69], v[66:67], off
	s_nop 0
	global_load_dwordx4 v[74:77], v[70:71], off
	v_mad_i64_i32 v[70:71], s[6:7], s38, 12, v[70:71]
	v_lshl_add_u64 v[78:79], v[70:71], 0, s[4:5]
	global_load_dwordx4 v[70:73], v[70:71], off
	s_nop 0
	global_load_dwordx4 v[82:85], v[78:79], off
	v_mad_i64_i32 v[78:79], s[6:7], s38, 12, v[78:79]
	v_lshl_add_u64 v[86:87], v[78:79], 0, s[4:5]
	global_load_dwordx4 v[78:81], v[78:79], off
	s_nop 0
	global_load_dwordx4 v[90:93], v[86:87], off
	v_mad_i64_i32 v[86:87], s[6:7], s38, 12, v[86:87]
	v_lshl_add_u64 v[94:95], v[86:87], 0, s[4:5]
	v_mad_i64_i32 v[102:103], s[6:7], s38, 12, v[94:95]
	global_load_dwordx4 v[86:89], v[86:87], off
	s_nop 0
	global_load_dwordx4 v[98:101], v[94:95], off
	s_cmp_eq_u64 s[34:35], 0
	global_load_dwordx4 v[94:97], v[102:103], off
	v_lshl_add_u64 v[102:103], v[102:103], 0, s[4:5]
	v_mad_i64_i32 v[110:111], s[6:7], s38, 12, v[102:103]
	global_load_dwordx4 v[106:109], v[102:103], off
	s_nop 0
	global_load_dwordx4 v[102:105], v[110:111], off
	v_lshl_add_u64 v[110:111], v[110:111], 0, s[4:5]
	v_mad_i64_i32 v[118:119], s[6:7], s38, 12, v[110:111]
	global_load_dwordx4 v[114:117], v[110:111], off
	s_nop 0
	global_load_dwordx4 v[110:113], v[118:119], off
	v_lshl_add_u64 v[118:119], v[118:119], 0, s[4:5]
	v_mad_i64_i32 v[126:127], s[6:7], s38, 12, v[118:119]
	global_load_dwordx4 v[122:125], v[118:119], off
	s_nop 0
	global_load_dwordx4 v[118:121], v[126:127], off
	v_lshl_add_u64 v[126:127], v[126:127], 0, s[4:5]
	global_load_dwordx4 v[126:129], v[126:127], off
	s_cbranch_scc1 .LBB0_614
	s_ashr_i32 s37, s36, 31
	s_lshl_b64 s[4:5], s[36:37], 2
	s_add_u32 s4, s34, s4
	s_addc_u32 s5, s35, s5
	v_lshlrev_b32_e32 v150, 2, v146
	s_mul_i32 s100, s98, 24
	global_load_dwordx2 v[152:153], v150, s[4:5]
	global_load_dwordx2 v[154:155], v150, s[4:5] offset:16
	global_load_dwordx2 v[156:157], v150, s[4:5] offset:32
	global_load_dwordx2 v[158:159], v150, s[4:5] offset:48
	global_load_dwordx2 v[160:161], v150, s[4:5] offset:64
	global_load_dwordx2 v[162:163], v150, s[4:5] offset:80
	global_load_dwordx2 v[164:165], v150, s[4:5] offset:96
	global_load_dwordx2 v[166:167], v150, s[4:5] offset:112
	s_branch .LBB0_615
.LBB0_614:
	s_mul_i32 s100, s98, 16
	v_mov_b32_e32 v153, 1.0
	v_mov_b32_e32 v152, v153
	v_mov_b32_e32 v155, v153
	v_mov_b32_e32 v154, v153
	v_mov_b32_e32 v157, v153
	v_mov_b32_e32 v156, v153
	v_mov_b32_e32 v159, v153
	v_mov_b32_e32 v158, v153
	v_mov_b32_e32 v161, v153
	v_mov_b32_e32 v160, v153
	v_mov_b32_e32 v163, v153
	v_mov_b32_e32 v162, v153
	v_mov_b32_e32 v165, v153
	v_mov_b32_e32 v164, v153
	v_mov_b32_e32 v167, v153
	v_mov_b32_e32 v166, v153
.LBB0_615:
	v_mov_b32_e32 v168, v6
	v_mov_b32_e32 v169, v2
	s_cmp_lt_u32 s100, 16
	s_cbranch_scc1 .Lcp_z0
	s_cmp_lt_u32 s100, 24
	s_cbranch_scc1 .Lcp_h0
	s_waitcnt vmcnt(39)
	s_branch .Lcp_j0
.Lcp_h0:
	s_waitcnt vmcnt(31)
	s_branch .Lcp_j0

; __device__ __forceinline__ unsigned pk_bf16(float lo, float hi) { const f32x2 f = {lo, hi}; const bf16v2 r = __builtin_convertvector(f, bf16v2); return __builtin_bit_cast(unsigned, r); }
; #define LAS __attribute__((address_space(3)))
; #define LAS __attribute__((address_space(3)))
; DI void witem_store(const WItem& d, const WRegs& R, LAS unsigned* scr, int lane) {
;     const int n4 = lane & 31, kh = lane >> 5;
; #pragma unroll
;     for (int i = 0; i < 8; ++i) {
;         v4u w; w.x = pk_bf16(R.a[i][0] * R.gg[i].x, R.b[i][0] * R.gg[i].y); w.y = pk_bf16(R.a[i][1] * R.gg[i].x, R.b[i][1] * R.gg[i].y);
;         w.z = pk_bf16(R.a[i][2] * R.gg[i].x, R.b[i][2] * R.gg[i].y); w.w = pk_bf16(R.a[i][3] * R.gg[i].x, R.b[i][3] * R.gg[i].y);
;         *(LAS v4u*)(scr + (2 * i + kh) * 132 + 4 * n4) = w; }
.Lcp_j0:
	v_pk_mul_f32 v[168:169], v[168:169], v[130:131]
	s_ashr_i32 s4, s44, 8
	v_cvt_pk_bf16_f32 v188, v168, v169
	v_mov_b32_e32 v168, v7
	v_mov_b32_e32 v169, v3
	v_pk_mul_f32 v[168:169], v[168:169], v[130:131]
	s_ashr_i32 s5, s45, 6
	v_cvt_pk_bf16_f32 v189, v168, v169
	v_mov_b32_e32 v168, v8
	v_mov_b32_e32 v169, v4
	v_pk_mul_f32 v[168:169], v[168:169], v[130:131]
	s_mul_i32 s4, s4, s5
	v_cvt_pk_bf16_f32 v190, v168, v169
	v_mov_b32_e32 v168, v9
	v_mov_b32_e32 v169, v5
	v_pk_mul_f32 v[168:169], v[168:169], v[130:131]
	s_ashr_i32 s5, s14, 6
	v_cvt_pk_bf16_f32 v191, v168, v169
	v_mov_b32_e32 v168, v14
	v_mov_b32_e32 v169, v10
	s_cmp_lt_u32 s100, 16
	s_cbranch_scc1 .Lcp_z1
	s_cmp_lt_u32 s100, 24
	s_cbranch_scc1 .Lcp_h1
	s_waitcnt vmcnt(38)
	s_branch .Lcp_j1
.Lcp_h1:
	s_waitcnt vmcnt(30)
	s_branch .Lcp_j1
.Lcp_z1:
	s_waitcnt vmcnt(14)
.Lcp_j1:
	v_pk_mul_f32 v[168:169], v[168:169], v[132:133]
	ds_write_b128 v186, v[188:191]
	v_cvt_pk_bf16_f32 v188, v168, v169
	v_mov_b32_e32 v168, v15
	v_mov_b32_e32 v169, v11
	v_pk_mul_f32 v[168:169], v[168:169], v[132:133]
	s_add_i32 s4, s5, s4
	v_cvt_pk_bf16_f32 v189, v168, v169
	v_mov_b32_e32 v168, v16
	v_mov_b32_e32 v169, v12
	v_pk_mul_f32 v[168:169], v[168:169], v[132:133]
	s_lshl_b32 s6, s44, 7
	v_cvt_pk_bf16_f32 v190, v168, v169
	v_mov_b32_e32 v168, v17
	v_mov_b32_e32 v169, v13
	v_pk_mul_f32 v[168:169], v[168:169], v[132:133]
	s_lshl_b32 s7, s14, 5
	v_cvt_pk_bf16_f32 v191, v168, v169
	v_mov_b32_e32 v168, v22
	v_mov_b32_e32 v169, v18
	s_cmp_lt_u32 s100, 16
	s_cbranch_scc1 .Lcp_z2
	s_cmp_lt_u32 s100, 24
	s_cbranch_scc1 .Lcp_h2
	s_waitcnt vmcnt(37)
	s_branch .Lcp_j2
.Lcp_h2:
	s_waitcnt vmcnt(29)
	s_branch .Lcp_j2
.Lcp_z2:
	s_waitcnt vmcnt(13)
.Lcp_j2:
	v_pk_mul_f32 v[168:169], v[168:169], v[134:135]
	ds_write_b128 v186, v[188:191] offset:1056
	v_cvt_pk_bf16_f32 v188, v168, v169
	v_mov_b32_e32 v168, v23
	v_mov_b32_e32 v169, v19
	v_pk_mul_f32 v[168:169], v[168:169], v[134:135]
	s_ashr_i32 s5, s4, 31
	v_cvt_pk_bf16_f32 v189, v168, v169
	v_mov_b32_e32 v168, v24
	v_mov_b32_e32 v169, v20
	v_pk_mul_f32 v[168:169], v[168:169], v[134:135]
	s_and_b32 s6, s6, 0x4000
	v_cvt_pk_bf16_f32 v190, v168, v169
	v_mov_b32_e32 v168, v25
	v_mov_b32_e32 v169, v21
	v_pk_mul_f32 v[168:169], v[168:169], v[134:135]
	s_and_b32 s7, s7, 0x400
	v_cvt_pk_bf16_f32 v191, v168, v169
	v_mov_b32_e32 v168, v30
	v_mov_b32_e32 v169, v26
	s_cmp_lt_u32 s100, 16
	s_cbranch_scc1 .Lcp_z3
	s_cmp_lt_u32 s100, 24
	s_cbranch_scc1 .Lcp_h3
	s_waitcnt vmcnt(36)
	s_branch .Lcp_j3
.Lcp_h3:
	s_waitcnt vmcnt(28)
	s_branch .Lcp_j3
.Lcp_z3:
	s_waitcnt vmcnt(12)
.Lcp_j3:
	v_pk_mul_f32 v[168:169], v[168:169], v[136:137]
	ds_write_b128 v186, v[188:191] offset:2112
	v_cvt_pk_bf16_f32 v188, v168, v169
	v_mov_b32_e32 v168, v31
	v_mov_b32_e32 v169, v27
	v_pk_mul_f32 v[168:169], v[168:169], v[136:137]
	s_lshl_b64 s[4:5], s[4:5], 15
	v_cvt_pk_bf16_f32 v189, v168, v169
	v_mov_b32_e32 v168, v32
	v_mov_b32_e32 v169, v28
	v_pk_mul_f32 v[168:169], v[168:169], v[136:137]
	s_or_b32 s15, s6, s7
	v_cvt_pk_bf16_f32 v190, v168, v169
	v_mov_b32_e32 v168, v33
	v_mov_b32_e32 v169, v29
	v_pk_mul_f32 v[168:169], v[168:169], v[136:137]
	v_cvt_pk_bf16_f32 v191, v168, v169
	v_mov_b32_e32 v168, v38
	v_mov_b32_e32 v169, v34
	s_cmp_lt_u32 s100, 16
	s_cbranch_scc1 .Lcp_z4
	s_cmp_lt_u32 s100, 24
	s_cbranch_scc1 .Lcp_h4
	s_waitcnt vmcnt(35)
	s_branch .Lcp_j4
.Lcp_h4:
	s_waitcnt vmcnt(27)
	s_branch .Lcp_j4
.Lcp_z4:
	s_waitcnt vmcnt(11)
.Lcp_j4:
	s_cmp_eq_u32 s48, 1
	v_pk_mul_f32 v[168:169], v[168:169], v[138:139]
	ds_write_b128 v186, v[188:191] offset:3168
	v_cvt_pk_bf16_f32 v188, v168, v169
	v_mov_b32_e32 v168, v39
	v_mov_b32_e32 v169, v35
	v_pk_mul_f32 v[168:169], v[168:169], v[138:139]
	s_cselect_b64 s[6:7], -1, 0
	v_cvt_pk_bf16_f32 v189, v168, v169
	v_mov_b32_e32 v168, v40
	v_mov_b32_e32 v169, v36
	v_pk_mul_f32 v[168:169], v[168:169], v[138:139]
	v_cndmask_b32_e64 v150, v149, v171, s[6:7]
	v_cvt_pk_bf16_f32 v190, v168, v169
	v_mov_b32_e32 v168, v41
	v_mov_b32_e32 v169, v37
	v_pk_mul_f32 v[168:169], v[168:169], v[138:139]
	v_lshl_add_u32 v150, v150, 2, v170
	v_cvt_pk_bf16_f32 v191, v168, v169
	v_mov_b32_e32 v168, v46
	v_mov_b32_e32 v169, v42
	s_cmp_lt_u32 s100, 16
	s_cbranch_scc1 .Lcp_z5
	s_cmp_lt_u32 s100, 24
	s_cbranch_scc1 .Lcp_h5
	s_waitcnt vmcnt(34)
	s_branch .Lcp_j5
.Lcp_h5:
	s_waitcnt vmcnt(26)
	s_branch .Lcp_j5
.Lcp_z5:
	s_waitcnt vmcnt(10)
.Lcp_j5:
	v_pk_mul_f32 v[168:169], v[168:169], v[140:141]
	ds_write_b128 v186, v[188:191] offset:4224
	v_cvt_pk_bf16_f32 v188, v168, v169
	v_mov_b32_e32 v168, v47
	v_mov_b32_e32 v169, v43
	v_pk_mul_f32 v[168:169], v[168:169], v[140:141]
	s_add_u32 s4, s12, s4
	v_cvt_pk_bf16_f32 v189, v168, v169
	v_mov_b32_e32 v168, v48
	v_mov_b32_e32 v169, v44
	v_pk_mul_f32 v[168:169], v[168:169], v[140:141]
	s_addc_u32 s5, s13, s5
	v_cvt_pk_bf16_f32 v190, v168, v169
	v_mov_b32_e32 v168, v49
	v_mov_b32_e32 v169, v45
	v_pk_mul_f32 v[168:169], v[168:169], v[140:141]
	v_cvt_pk_bf16_f32 v191, v168, v169
	v_mov_b32_e32 v168, v54
	v_mov_b32_e32 v169, v50
	s_cmp_lt_u32 s100, 16
	s_cbranch_scc1 .Lcp_z6
	s_cmp_lt_u32 s100, 24
	s_cbranch_scc1 .Lcp_h6
	s_waitcnt vmcnt(33)
	s_branch .Lcp_j6
.Lcp_h6:
	s_waitcnt vmcnt(25)
	s_branch .Lcp_j6
.Lcp_z6:
	s_waitcnt vmcnt(9)
.Lcp_j6:
	v_pk_mul_f32 v[168:169], v[168:169], v[142:143]
	ds_write_b128 v186, v[188:191] offset:5280
	v_cvt_pk_bf16_f32 v188, v168, v169
	v_mov_b32_e32 v168, v55
	v_mov_b32_e32 v169, v51
	v_pk_mul_f32 v[168:169], v[168:169], v[142:143]
	s_nop 0
	v_cvt_pk_bf16_f32 v189, v168, v169
	v_mov_b32_e32 v168, v56
	v_mov_b32_e32 v169, v52
	v_pk_mul_f32 v[168:169], v[168:169], v[142:143]
	s_nop 0
	v_cvt_pk_bf16_f32 v190, v168, v169
	v_mov_b32_e32 v168, v57
	v_mov_b32_e32 v169, v53
	v_pk_mul_f32 v[168:169], v[168:169], v[142:143]
	s_nop 0
	v_cvt_pk_bf16_f32 v191, v168, v169
	v_mov_b32_e32 v168, v62
	s_cmp_lt_u32 s100, 16
	s_cbranch_scc1 .Lcp_z7
	s_cmp_lt_u32 s100, 24
	s_cbranch_scc1 .Lcp_h7
	s_waitcnt vmcnt(32)
	s_branch .Lcp_j7
.Lcp_h7:
	s_waitcnt vmcnt(24)
	s_branch .Lcp_j7

; __device__ __forceinline__ unsigned pk_bf16(float lo, float hi) { const f32x2 f = {lo, hi}; const bf16v2 r = __builtin_convertvector(f, bf16v2); return __builtin_bit_cast(unsigned, r); }
; #define LAS __attribute__((address_space(3)))
; #define GAS __attribute__((address_space(1)))
; #define LAS __attribute__((address_space(3)))
; #define LDS_WAIT() asm volatile("s_waitcnt lgkmcnt(0)" ::: "memory")
; DI void witem_store(const WItem& d, const WRegs& R, LAS unsigned* scr, int lane) {
;     ...
;     for (int i = 0; i < 8; ++i) {
;         v4u w; w.x = pk_bf16(R.a[i][0] * R.gg[i].x, R.b[i][0] * R.gg[i].y); w.y = pk_bf16(R.a[i][1] * R.gg[i].x, R.b[i][1] * R.gg[i].y);
;         w.z = pk_bf16(R.a[i][2] * R.gg[i].x, R.b[i][2] * R.gg[i].y); w.w = pk_bf16(R.a[i][3] * R.gg[i].x, R.b[i][3] * R.gg[i].y);
;         *(LAS v4u*)(scr + (2 * i + kh) * 132 + 4 * n4) = w; }
;     LDS_WAIT(); asm volatile("" ::: "memory");
;     const int bb = 16 * lane, ob = bb ^ (((bb >> 9) & 1) << 5), rr = ob >> 6, kp0 = (ob & 63) >> 2;
;     const size_t base = ((size_t)((d.dst_row0 >> 8) * (d.Kd >> 6) + (d.k0 >> 6)) * 32768 + (size_t)(((d.dst_row0 >> 7) & 1) * 16384 + ((d.k0 >> 5) & 1) * 1024 + bb)) >> 1;
; #pragma unroll
;     for (int grp = 0; grp < 8; ++grp) {
;         const int Rs = 16 * grp + rr, nloc = d.perm == 2 ? pg8::permrow<2>(Rs) : d.perm == 1 ? pg8::permrow<1>(Rs) : Rs;
;         const LAS unsigned* sp = scr + kp0 * 132 + nloc;
;         v4u o; o.x = sp[0]; o.y = sp[132]; o.z = sp[264]; o.w = sp[396];
;         *(GAS v4u*)(d.WT + base + (size_t)grp * 1024) = o;
;     }
;     LDS_WAIT(); asm volatile("" ::: "memory");
.Lcp_j7:
	s_cmp_lt_i32 s48, 2
	v_mov_b32_e32 v169, v58
	v_pk_mul_f32 v[168:169], v[168:169], v[144:145]
	ds_write_b128 v186, v[188:191] offset:6336
	v_cvt_pk_bf16_f32 v188, v168, v169
	v_mov_b32_e32 v168, v63
	v_mov_b32_e32 v169, v59
	v_pk_mul_f32 v[168:169], v[168:169], v[144:145]
	s_nop 0
	v_cvt_pk_bf16_f32 v189, v168, v169
	v_mov_b32_e32 v168, v64
	v_mov_b32_e32 v169, v60
	v_pk_mul_f32 v[168:169], v[168:169], v[144:145]
	s_nop 0
	v_cvt_pk_bf16_f32 v190, v168, v169
	v_mov_b32_e32 v168, v65
	v_mov_b32_e32 v169, v61
	v_pk_mul_f32 v[168:169], v[168:169], v[144:145]
	s_nop 0
	v_cvt_pk_bf16_f32 v191, v168, v169
	ds_write_b128 v186, v[188:191] offset:7392
	s_waitcnt lgkmcnt(0)
	ds_read2_b32 v[188:189], v150 offset1:132
	v_add_u32_e32 v150, 0x400, v150
	ds_read2_b32 v[190:191], v150 offset0:8 offset1:140
	v_or_b32_e32 v150, s15, v147
	v_lshl_add_u64 v[168:169], s[4:5], 0, v[150:151]
	s_waitcnt lgkmcnt(0)
	global_store_dwordx4 v150, v[188:191], s[4:5]
	s_mov_b64 s[4:5], -1
	s_cbranch_scc1 .LBB0_619
	s_cmp_eq_u32 s48, 2
	v_mov_b32_e32 v150, v172
	s_cbranch_scc0 .LBB0_618
	v_mov_b32_e32 v150, v174

; #define GAS __attribute__((address_space(1)))
; template <bool UNCOND> DI void witem_load(const WItem& d, WRegs& R, int lane) {
;     const int n4 = lane & 31, kh = lane >> 5;
;     const float* src = d.W + (size_t)(d.k0 + 2 * kh) * d.N + d.src_col0 + 4 * n4;
; #pragma unroll
;     for (int i = 0; i < 8; ++i) { R.a[i] = *(const GAS f32x4*)(src + (size_t)(4 * i) * d.N); R.b[i] = *(const GAS f32x4*)(src + (size_t)(4 * i + 1) * d.N); }
;     if (UNCOND) {
;         const float* gp = d.gain ? d.gain + d.k0 + 2 * kh : src;
; #pragma unroll
;         for (int i = 0; i < 8; ++i) R.gg[i] = *(const GAS f32x2g*)(gp + 4 * i);
;         if (!d.gain) {
; #pragma unroll
;             for (int i = 0; i < 8; ++i) R.gg[i] = (f32x2g){1.f, 1.f}; }
;     } else if (d.gain) {
; #pragma unroll
;         for (int i = 0; i < 8; ++i) R.gg[i] = *(const GAS f32x2g*)(d.gain + d.k0 + 4 * i + 2 * kh); }
;     else {
; #pragma unroll
;         for (int i = 0; i < 8; ++i) R.gg[i] = (f32x2g){1.f, 1.f}; }
; }
.LBB0_679:
	s_andn2_b64 vcc, exec, s[0:1]
	s_mov_b32 s100, 0
	s_cbranch_vccnz .LBB0_683
	v_add_u32_e32 v2, s14, v146
	v_mad_i64_i32 v[2:3], s[0:1], s16, v2, 0
	v_lshl_add_u64 v[2:3], v[2:3], 2, s[8:9]
	s_ashr_i32 s19, s18, 31
	s_ashr_i32 s17, s16, 31
	v_lshl_add_u64 v[2:3], s[18:19], 2, v[2:3]
	v_lshlrev_b32_e32 v150, 2, v148
	v_lshl_add_u64 v[2:3], v[2:3], 0, v[150:151]
	s_lshl_b64 s[0:1], s[16:17], 2
	v_lshl_add_u64 v[10:11], v[2:3], 0, s[0:1]
	global_load_dwordx4 v[6:9], v[2:3], off
	s_nop 0
	global_load_dwordx4 v[2:5], v[10:11], off
	v_mad_i64_i32 v[10:11], s[4:5], s16, 12, v[10:11]
	v_lshl_add_u64 v[18:19], v[10:11], 0, s[0:1]
	global_load_dwordx4 v[14:17], v[10:11], off
	s_nop 0
	global_load_dwordx4 v[10:13], v[18:19], off
	v_mad_i64_i32 v[18:19], s[4:5], s16, 12, v[18:19]
	v_lshl_add_u64 v[26:27], v[18:19], 0, s[0:1]
	global_load_dwordx4 v[22:25], v[18:19], off
	s_nop 0
	global_load_dwordx4 v[18:21], v[26:27], off
	v_mad_i64_i32 v[26:27], s[4:5], s16, 12, v[26:27]
	v_lshl_add_u64 v[34:35], v[26:27], 0, s[0:1]
	global_load_dwordx4 v[30:33], v[26:27], off
	s_nop 0
	global_load_dwordx4 v[26:29], v[34:35], off
	v_mad_i64_i32 v[34:35], s[4:5], s16, 12, v[34:35]
	v_lshl_add_u64 v[42:43], v[34:35], 0, s[0:1]
	global_load_dwordx4 v[38:41], v[34:35], off
	s_cmp_eq_u64 s[10:11], 0
	global_load_dwordx4 v[34:37], v[42:43], off
	v_mad_i64_i32 v[42:43], s[4:5], s16, 12, v[42:43]
	v_lshl_add_u64 v[50:51], v[42:43], 0, s[0:1]
	global_load_dwordx4 v[46:49], v[42:43], off
	s_nop 0
	global_load_dwordx4 v[42:45], v[50:51], off
	v_mad_i64_i32 v[50:51], s[4:5], s16, 12, v[50:51]
	v_lshl_add_u64 v[58:59], v[50:51], 0, s[0:1]
	global_load_dwordx4 v[54:57], v[50:51], off
	s_nop 0
	global_load_dwordx4 v[50:53], v[58:59], off
	v_mad_i64_i32 v[58:59], s[4:5], s16, 12, v[58:59]
	global_load_dwordx4 v[62:65], v[58:59], off
	v_lshl_add_u64 v[58:59], v[58:59], 0, s[0:1]
	global_load_dwordx4 v[58:61], v[58:59], off
	s_cbranch_scc1 .LBB0_682
	s_ashr_i32 s15, s14, 31
	s_lshl_b64 s[0:1], s[14:15], 2
	s_add_u32 s0, s10, s0
	s_addc_u32 s1, s11, s1
	v_lshlrev_b32_e32 v144, 2, v146
	s_mul_i32 s100, s98, 24
	global_load_dwordx2 v[130:131], v144, s[0:1]
	global_load_dwordx2 v[132:133], v144, s[0:1] offset:16
	global_load_dwordx2 v[134:135], v144, s[0:1] offset:32
	global_load_dwordx2 v[136:137], v144, s[0:1] offset:48
	global_load_dwordx2 v[138:139], v144, s[0:1] offset:64
	global_load_dwordx2 v[140:141], v144, s[0:1] offset:80
	global_load_dwordx2 v[142:143], v144, s[0:1] offset:96
	s_nop 0
	global_load_dwordx2 v[144:145], v144, s[0:1] offset:112
	s_branch .LBB0_683
.LBB0_682:
	s_mul_i32 s100, s98, 16
	v_mov_b32_e32 v131, 1.0
	v_mov_b32_e32 v130, v131
	v_mov_b32_e32 v133, v131
	v_mov_b32_e32 v132, v131
	v_mov_b32_e32 v135, v131
	v_mov_b32_e32 v134, v131
	v_mov_b32_e32 v137, v131
	v_mov_b32_e32 v136, v131
	v_mov_b32_e32 v139, v131
	v_mov_b32_e32 v138, v131
	v_mov_b32_e32 v141, v131
	v_mov_b32_e32 v140, v131
	v_mov_b32_e32 v143, v131
	v_mov_b32_e32 v142, v131
	v_mov_b32_e32 v145, v131
	v_mov_b32_e32 v144, v131
.LBB0_683:
	s_cmp_lt_u32 s100, 16
	s_cbranch_scc1 .Lcp_z8
	s_cmp_lt_u32 s100, 24
	s_cbranch_scc1 .Lcp_h8
	s_waitcnt vmcnt(47)
	s_branch .Lcp_j8
.Lcp_h8:
	s_waitcnt vmcnt(39)
	s_branch .Lcp_j8

; __device__ __forceinline__ unsigned pk_bf16(float lo, float hi) { const f32x2 f = {lo, hi}; const bf16v2 r = __builtin_convertvector(f, bf16v2); return __builtin_bit_cast(unsigned, r); }
; #define LAS __attribute__((address_space(3)))
; #define LAS __attribute__((address_space(3)))
; DI void witem_store(const WItem& d, const WRegs& R, LAS unsigned* scr, int lane) {
;     ...
;     for (int i = 0; i < 8; ++i) {
;         v4u w; w.x = pk_bf16(R.a[i][0] * R.gg[i].x, R.b[i][0] * R.gg[i].y); w.y = pk_bf16(R.a[i][1] * R.gg[i].x, R.b[i][1] * R.gg[i].y);
;         w.z = pk_bf16(R.a[i][2] * R.gg[i].x, R.b[i][2] * R.gg[i].y); w.w = pk_bf16(R.a[i][3] * R.gg[i].x, R.b[i][3] * R.gg[i].y);
;         *(LAS v4u*)(scr + (2 * i + kh) * 132 + 4 * n4) = w; }
.Lcp_j8:
	v_mov_b32_e32 v168, v66
	s_cmp_lt_u32 s100, 16
	s_cbranch_scc1 .Lcp_z9
	s_cmp_lt_u32 s100, 24
	s_cbranch_scc1 .Lcp_h9
	s_waitcnt vmcnt(46)
	s_branch .Lcp_j9
.Lcp_h9:
	s_waitcnt vmcnt(38)
	s_branch .Lcp_j9
.Lcp_z9:
	s_waitcnt vmcnt(22)
.Lcp_j9:
	v_mov_b32_e32 v169, v74
	s_cmp_lt_u32 s100, 16
	s_cbranch_scc1 .Lcp_z10
	s_cmp_lt_u32 s100, 24
	s_cbranch_scc1 .Lcp_h10
	s_waitcnt vmcnt(39)
	s_branch .Lcp_j10

; __device__ __forceinline__ unsigned pk_bf16(float lo, float hi) { const f32x2 f = {lo, hi}; const bf16v2 r = __builtin_convertvector(f, bf16v2); return __builtin_bit_cast(unsigned, r); }
; #define LAS __attribute__((address_space(3)))
; #define LAS __attribute__((address_space(3)))
; DI void witem_store(const WItem& d, const WRegs& R, LAS unsigned* scr, int lane) {
;     ...
;     for (int i = 0; i < 8; ++i) {
;         v4u w; w.x = pk_bf16(R.a[i][0] * R.gg[i].x, R.b[i][0] * R.gg[i].y); w.y = pk_bf16(R.a[i][1] * R.gg[i].x, R.b[i][1] * R.gg[i].y);
;         w.z = pk_bf16(R.a[i][2] * R.gg[i].x, R.b[i][2] * R.gg[i].y); w.w = pk_bf16(R.a[i][3] * R.gg[i].x, R.b[i][3] * R.gg[i].y);
;         *(LAS v4u*)(scr + (2 * i + kh) * 132 + 4 * n4) = w; }
.Lcp_j10:
	v_pk_mul_f32 v[168:169], v[152:153], v[168:169]
	s_ashr_i32 s0, s81, 8
	v_cvt_pk_bf16_f32 v188, v168, v169
	v_mov_b32_e32 v168, v67
	v_mov_b32_e32 v169, v75
	v_pk_mul_f32 v[168:169], v[152:153], v[168:169]
	s_ashr_i32 s1, s86, 6
	v_cvt_pk_bf16_f32 v189, v168, v169
	v_mov_b32_e32 v168, v68
	v_mov_b32_e32 v169, v76
	v_pk_mul_f32 v[168:169], v[152:153], v[168:169]
	s_mul_i32 s0, s1, s0
	v_cvt_pk_bf16_f32 v190, v168, v169
	v_mov_b32_e32 v168, v69
	v_mov_b32_e32 v169, v77
	v_pk_mul_f32 v[168:169], v[152:153], v[168:169]
	s_ashr_i32 s1, s36, 6
	v_cvt_pk_bf16_f32 v191, v168, v169
	v_mov_b32_e32 v168, v70
	v_mov_b32_e32 v169, v82
	s_cmp_lt_u32 s100, 16
	s_cbranch_scc1 .Lcp_z11
	s_cmp_lt_u32 s100, 24
	s_cbranch_scc1 .Lcp_h11
	s_waitcnt vmcnt(38)
	s_branch .Lcp_j11

; __device__ __forceinline__ unsigned pk_bf16(float lo, float hi) { const f32x2 f = {lo, hi}; const bf16v2 r = __builtin_convertvector(f, bf16v2); return __builtin_bit_cast(unsigned, r); }
; #define LAS __attribute__((address_space(3)))
; #define LAS __attribute__((address_space(3)))
; DI void witem_store(const WItem& d, const WRegs& R, LAS unsigned* scr, int lane) {
;     ...
;     for (int i = 0; i < 8; ++i) {
;         v4u w; w.x = pk_bf16(R.a[i][0] * R.gg[i].x, R.b[i][0] * R.gg[i].y); w.y = pk_bf16(R.a[i][1] * R.gg[i].x, R.b[i][1] * R.gg[i].y);
;         w.z = pk_bf16(R.a[i][2] * R.gg[i].x, R.b[i][2] * R.gg[i].y); w.w = pk_bf16(R.a[i][3] * R.gg[i].x, R.b[i][3] * R.gg[i].y);
;         *(LAS v4u*)(scr + (2 * i + kh) * 132 + 4 * n4) = w; }
.Lcp_j11:
	v_pk_mul_f32 v[168:169], v[154:155], v[168:169]
	ds_write_b128 v186, v[188:191]
	v_cvt_pk_bf16_f32 v188, v168, v169
	v_mov_b32_e32 v168, v71
	v_mov_b32_e32 v169, v83
	v_pk_mul_f32 v[168:169], v[154:155], v[168:169]
	s_add_i32 s0, s0, s1
	v_cvt_pk_bf16_f32 v189, v168, v169
	v_mov_b32_e32 v168, v72
	v_mov_b32_e32 v169, v84
	v_pk_mul_f32 v[168:169], v[154:155], v[168:169]
	s_ashr_i32 s1, s0, 31
	v_cvt_pk_bf16_f32 v190, v168, v169
	v_mov_b32_e32 v168, v73
	v_mov_b32_e32 v169, v85
	v_pk_mul_f32 v[168:169], v[154:155], v[168:169]
	s_lshl_b64 s[4:5], s[0:1], 15
	v_cvt_pk_bf16_f32 v191, v168, v169
	v_mov_b32_e32 v168, v78
	v_mov_b32_e32 v169, v90
	s_cmp_lt_u32 s100, 16
	s_cbranch_scc1 .Lcp_z12
	s_cmp_lt_u32 s100, 24
	s_cbranch_scc1 .Lcp_h12
	s_waitcnt vmcnt(37)
	s_branch .Lcp_j12

; __device__ __forceinline__ unsigned pk_bf16(float lo, float hi) { const f32x2 f = {lo, hi}; const bf16v2 r = __builtin_convertvector(f, bf16v2); return __builtin_bit_cast(unsigned, r); }
; #define LAS __attribute__((address_space(3)))
; #define LAS __attribute__((address_space(3)))
; DI void witem_store(const WItem& d, const WRegs& R, LAS unsigned* scr, int lane) {
;     ...
;     for (int i = 0; i < 8; ++i) {
;         v4u w; w.x = pk_bf16(R.a[i][0] * R.gg[i].x, R.b[i][0] * R.gg[i].y); w.y = pk_bf16(R.a[i][1] * R.gg[i].x, R.b[i][1] * R.gg[i].y);
;         w.z = pk_bf16(R.a[i][2] * R.gg[i].x, R.b[i][2] * R.gg[i].y); w.w = pk_bf16(R.a[i][3] * R.gg[i].x, R.b[i][3] * R.gg[i].y);
;         *(LAS v4u*)(scr + (2 * i + kh) * 132 + 4 * n4) = w; }
.Lcp_j12:
	v_pk_mul_f32 v[168:169], v[156:157], v[168:169]
	ds_write_b128 v186, v[188:191] offset:1056
	v_cvt_pk_bf16_f32 v188, v168, v169
	v_mov_b32_e32 v168, v79
	v_mov_b32_e32 v169, v91
	v_pk_mul_f32 v[168:169], v[156:157], v[168:169]
	s_lshl_b32 s0, s81, 7
	v_cvt_pk_bf16_f32 v189, v168, v169
	v_mov_b32_e32 v168, v80
	v_mov_b32_e32 v169, v92
	v_pk_mul_f32 v[168:169], v[156:157], v[168:169]
	s_lshl_b32 s1, s36, 5
	v_cvt_pk_bf16_f32 v190, v168, v169
	v_mov_b32_e32 v168, v81
	v_mov_b32_e32 v169, v93
	v_pk_mul_f32 v[168:169], v[156:157], v[168:169]
	s_and_b32 s0, s0, 0x4000
	v_cvt_pk_bf16_f32 v191, v168, v169
	v_mov_b32_e32 v168, v86
	v_mov_b32_e32 v169, v98
	s_cmp_lt_u32 s100, 16
	s_cbranch_scc1 .Lcp_z13
	s_cmp_lt_u32 s100, 24
	s_cbranch_scc1 .Lcp_h13
	s_waitcnt vmcnt(36)
	s_branch .Lcp_j13

; __device__ __forceinline__ unsigned pk_bf16(float lo, float hi) { const f32x2 f = {lo, hi}; const bf16v2 r = __builtin_convertvector(f, bf16v2); return __builtin_bit_cast(unsigned, r); }
; #define LAS __attribute__((address_space(3)))
; #define LAS __attribute__((address_space(3)))
; DI void witem_store(const WItem& d, const WRegs& R, LAS unsigned* scr, int lane) {
;     ...
;     for (int i = 0; i < 8; ++i) {
;         v4u w; w.x = pk_bf16(R.a[i][0] * R.gg[i].x, R.b[i][0] * R.gg[i].y); w.y = pk_bf16(R.a[i][1] * R.gg[i].x, R.b[i][1] * R.gg[i].y);
;         w.z = pk_bf16(R.a[i][2] * R.gg[i].x, R.b[i][2] * R.gg[i].y); w.w = pk_bf16(R.a[i][3] * R.gg[i].x, R.b[i][3] * R.gg[i].y);
;         *(LAS v4u*)(scr + (2 * i + kh) * 132 + 4 * n4) = w; }
.Lcp_j13:
	v_pk_mul_f32 v[168:169], v[158:159], v[168:169]
	ds_write_b128 v186, v[188:191] offset:2112
	v_cvt_pk_bf16_f32 v188, v168, v169
	v_mov_b32_e32 v168, v87
	v_mov_b32_e32 v169, v99
	v_pk_mul_f32 v[168:169], v[158:159], v[168:169]
	s_and_b32 s1, s1, 0x400
	v_cvt_pk_bf16_f32 v189, v168, v169
	v_mov_b32_e32 v168, v88
	v_mov_b32_e32 v169, v100
	v_pk_mul_f32 v[168:169], v[158:159], v[168:169]
	s_or_b32 s15, s1, s0
	v_cvt_pk_bf16_f32 v190, v168, v169
	v_mov_b32_e32 v168, v89
	v_mov_b32_e32 v169, v101
	v_pk_mul_f32 v[168:169], v[158:159], v[168:169]
	v_cvt_pk_bf16_f32 v191, v168, v169
	v_mov_b32_e32 v168, v94
	v_mov_b32_e32 v169, v106
	s_cmp_lt_u32 s100, 16
	s_cbranch_scc1 .Lcp_z14
	s_cmp_lt_u32 s100, 24
	s_cbranch_scc1 .Lcp_h14
	s_waitcnt vmcnt(35)
	s_branch .Lcp_j14

; __device__ __forceinline__ unsigned pk_bf16(float lo, float hi) { const f32x2 f = {lo, hi}; const bf16v2 r = __builtin_convertvector(f, bf16v2); return __builtin_bit_cast(unsigned, r); }
; #define LAS __attribute__((address_space(3)))
; #define LAS __attribute__((address_space(3)))
; DI void witem_store(const WItem& d, const WRegs& R, LAS unsigned* scr, int lane) {
;     ...
;     for (int i = 0; i < 8; ++i) {
;         v4u w; w.x = pk_bf16(R.a[i][0] * R.gg[i].x, R.b[i][0] * R.gg[i].y); w.y = pk_bf16(R.a[i][1] * R.gg[i].x, R.b[i][1] * R.gg[i].y);
;         w.z = pk_bf16(R.a[i][2] * R.gg[i].x, R.b[i][2] * R.gg[i].y); w.w = pk_bf16(R.a[i][3] * R.gg[i].x, R.b[i][3] * R.gg[i].y);
;         *(LAS v4u*)(scr + (2 * i + kh) * 132 + 4 * n4) = w; }
.Lcp_j14:
	s_cmp_eq_u32 s87, 1
	v_pk_mul_f32 v[168:169], v[160:161], v[168:169]
	ds_write_b128 v186, v[188:191] offset:3168
	v_cvt_pk_bf16_f32 v188, v168, v169
	v_mov_b32_e32 v168, v95
	v_mov_b32_e32 v169, v107
	v_pk_mul_f32 v[168:169], v[160:161], v[168:169]
	s_cselect_b64 s[0:1], -1, 0
	v_cvt_pk_bf16_f32 v189, v168, v169
	v_mov_b32_e32 v168, v96
	v_mov_b32_e32 v169, v108
	v_pk_mul_f32 v[168:169], v[160:161], v[168:169]
	v_cndmask_b32_e64 v150, v149, v171, s[0:1]
	v_cvt_pk_bf16_f32 v190, v168, v169
	v_mov_b32_e32 v168, v97
	v_mov_b32_e32 v169, v109
	v_pk_mul_f32 v[168:169], v[160:161], v[168:169]
	v_lshl_add_u32 v150, v150, 2, v170
	v_cvt_pk_bf16_f32 v191, v168, v169
	v_mov_b32_e32 v168, v102
	v_mov_b32_e32 v169, v114
	s_cmp_lt_u32 s100, 16
	s_cbranch_scc1 .Lcp_z15
	s_cmp_lt_u32 s100, 24
	s_cbranch_scc1 .Lcp_h15
	s_waitcnt vmcnt(34)
	s_branch .Lcp_j15

; __device__ __forceinline__ unsigned pk_bf16(float lo, float hi) { const f32x2 f = {lo, hi}; const bf16v2 r = __builtin_convertvector(f, bf16v2); return __builtin_bit_cast(unsigned, r); }
; #define LAS __attribute__((address_space(3)))
; #define LAS __attribute__((address_space(3)))
; DI void witem_store(const WItem& d, const WRegs& R, LAS unsigned* scr, int lane) {
;     ...
;     for (int i = 0; i < 8; ++i) {
;         v4u w; w.x = pk_bf16(R.a[i][0] * R.gg[i].x, R.b[i][0] * R.gg[i].y); w.y = pk_bf16(R.a[i][1] * R.gg[i].x, R.b[i][1] * R.gg[i].y);
;         w.z = pk_bf16(R.a[i][2] * R.gg[i].x, R.b[i][2] * R.gg[i].y); w.w = pk_bf16(R.a[i][3] * R.gg[i].x, R.b[i][3] * R.gg[i].y);
;         *(LAS v4u*)(scr + (2 * i + kh) * 132 + 4 * n4) = w; }
.Lcp_j15:
	v_pk_mul_f32 v[168:169], v[162:163], v[168:169]
	ds_write_b128 v186, v[188:191] offset:4224
	v_cvt_pk_bf16_f32 v188, v168, v169
	v_mov_b32_e32 v168, v103
	v_mov_b32_e32 v169, v115
	v_pk_mul_f32 v[168:169], v[162:163], v[168:169]
	s_add_u32 s4, s40, s4
	v_cvt_pk_bf16_f32 v189, v168, v169
	v_mov_b32_e32 v168, v104
	v_mov_b32_e32 v169, v116
	v_pk_mul_f32 v[168:169], v[162:163], v[168:169]
	s_addc_u32 s5, s41, s5
	v_cvt_pk_bf16_f32 v190, v168, v169
	v_mov_b32_e32 v168, v105
	v_mov_b32_e32 v169, v117
	v_pk_mul_f32 v[168:169], v[162:163], v[168:169]
	v_cvt_pk_bf16_f32 v191, v168, v169
	v_mov_b32_e32 v168, v110
	v_mov_b32_e32 v169, v122
	s_cmp_lt_u32 s100, 16
	s_cbranch_scc1 .Lcp_z16
	s_cmp_lt_u32 s100, 24
	s_cbranch_scc1 .Lcp_h16
	s_waitcnt vmcnt(33)
	s_branch .Lcp_j16

; __device__ __forceinline__ unsigned pk_bf16(float lo, float hi) { const f32x2 f = {lo, hi}; const bf16v2 r = __builtin_convertvector(f, bf16v2); return __builtin_bit_cast(unsigned, r); }
; #define LAS __attribute__((address_space(3)))
; #define LAS __attribute__((address_space(3)))
; DI void witem_store(const WItem& d, const WRegs& R, LAS unsigned* scr, int lane) {
;     ...
;     for (int i = 0; i < 8; ++i) {
;         v4u w; w.x = pk_bf16(R.a[i][0] * R.gg[i].x, R.b[i][0] * R.gg[i].y); w.y = pk_bf16(R.a[i][1] * R.gg[i].x, R.b[i][1] * R.gg[i].y);
;         w.z = pk_bf16(R.a[i][2] * R.gg[i].x, R.b[i][2] * R.gg[i].y); w.w = pk_bf16(R.a[i][3] * R.gg[i].x, R.b[i][3] * R.gg[i].y);
;         *(LAS v4u*)(scr + (2 * i + kh) * 132 + 4 * n4) = w; }
.Lcp_j16:
	v_pk_mul_f32 v[168:169], v[164:165], v[168:169]
	ds_write_b128 v186, v[188:191] offset:5280
	v_cvt_pk_bf16_f32 v188, v168, v169
	v_mov_b32_e32 v168, v111
	v_mov_b32_e32 v169, v123
	v_pk_mul_f32 v[168:169], v[164:165], v[168:169]
	s_nop 0
	v_cvt_pk_bf16_f32 v189, v168, v169
	v_mov_b32_e32 v168, v112
	v_mov_b32_e32 v169, v124
	v_pk_mul_f32 v[168:169], v[164:165], v[168:169]
	s_nop 0
	v_cvt_pk_bf16_f32 v190, v168, v169
	v_mov_b32_e32 v168, v113
	v_mov_b32_e32 v169, v125
	v_pk_mul_f32 v[168:169], v[164:165], v[168:169]
	s_nop 0
	v_cvt_pk_bf16_f32 v191, v168, v169
	v_mov_b32_e32 v168, v118
	s_cmp_lt_u32 s100, 16
	s_cbranch_scc1 .Lcp_z17
	s_cmp_lt_u32 s100, 24
	s_cbranch_scc1 .Lcp_h17
	s_waitcnt vmcnt(32)
	s_branch .Lcp_j17

; __device__ __forceinline__ unsigned pk_bf16(float lo, float hi) { const f32x2 f = {lo, hi}; const bf16v2 r = __builtin_convertvector(f, bf16v2); return __builtin_bit_cast(unsigned, r); }
; #define LAS __attribute__((address_space(3)))
; #define GAS __attribute__((address_space(1)))
; #define LAS __attribute__((address_space(3)))
; #define LDS_WAIT() asm volatile("s_waitcnt lgkmcnt(0)" ::: "memory")
; DI void witem_store(const WItem& d, const WRegs& R, LAS unsigned* scr, int lane) {
;     ...
;     for (int i = 0; i < 8; ++i) {
;         v4u w; w.x = pk_bf16(R.a[i][0] * R.gg[i].x, R.b[i][0] * R.gg[i].y); w.y = pk_bf16(R.a[i][1] * R.gg[i].x, R.b[i][1] * R.gg[i].y);
;         w.z = pk_bf16(R.a[i][2] * R.gg[i].x, R.b[i][2] * R.gg[i].y); w.w = pk_bf16(R.a[i][3] * R.gg[i].x, R.b[i][3] * R.gg[i].y);
;         *(LAS v4u*)(scr + (2 * i + kh) * 132 + 4 * n4) = w; }
;     LDS_WAIT(); asm volatile("" ::: "memory");
;     const int bb = 16 * lane, ob = bb ^ (((bb >> 9) & 1) << 5), rr = ob >> 6, kp0 = (ob & 63) >> 2;
;     const size_t base = ((size_t)((d.dst_row0 >> 8) * (d.Kd >> 6) + (d.k0 >> 6)) * 32768 + (size_t)(((d.dst_row0 >> 7) & 1) * 16384 + ((d.k0 >> 5) & 1) * 1024 + bb)) >> 1;
; #pragma unroll
;     for (int grp = 0; grp < 8; ++grp) {
;         const int Rs = 16 * grp + rr, nloc = d.perm == 2 ? pg8::permrow<2>(Rs) : d.perm == 1 ? pg8::permrow<1>(Rs) : Rs;
;         const LAS unsigned* sp = scr + kp0 * 132 + nloc;
;         v4u o; o.x = sp[0]; o.y = sp[132]; o.z = sp[264]; o.w = sp[396];
;         *(GAS v4u*)(d.WT + base + (size_t)grp * 1024) = o;
;     }
;     LDS_WAIT(); asm volatile("" ::: "memory");
.Lcp_j17:
	s_cmp_lt_i32 s87, 2
	v_mov_b32_e32 v169, v126
	v_pk_mul_f32 v[168:169], v[166:167], v[168:169]
	ds_write_b128 v186, v[188:191] offset:6336
	v_cvt_pk_bf16_f32 v188, v168, v169
	v_mov_b32_e32 v168, v119
	v_mov_b32_e32 v169, v127
	v_pk_mul_f32 v[168:169], v[166:167], v[168:169]
	s_nop 0
	v_cvt_pk_bf16_f32 v189, v168, v169
	v_mov_b32_e32 v168, v120
	v_mov_b32_e32 v169, v128
	v_pk_mul_f32 v[168:169], v[166:167], v[168:169]
	s_nop 0
	v_cvt_pk_bf16_f32 v190, v168, v169
	v_mov_b32_e32 v168, v121
	v_mov_b32_e32 v169, v129
	v_pk_mul_f32 v[168:169], v[166:167], v[168:169]
	s_nop 0
	v_cvt_pk_bf16_f32 v191, v168, v169
	ds_write_b128 v186, v[188:191] offset:7392
	s_waitcnt lgkmcnt(0)
	ds_read2_b32 v[188:189], v150 offset1:132
	v_add_u32_e32 v150, 0x400, v150
	ds_read2_b32 v[190:191], v150 offset0:8 offset1:140
	v_or_b32_e32 v150, s15, v147
	v_lshl_add_u64 v[168:169], s[4:5], 0, v[150:151]
	s_waitcnt lgkmcnt(0)
	global_store_dwordx4 v150, v[188:191], s[4:5]
	s_mov_b64 s[4:5], -1
	s_cbranch_scc1 .LBB0_687
	s_cmp_eq_u32 s87, 2
	v_mov_b32_e32 v150, v172
	s_cbranch_scc0 .LBB0_686
	v_mov_b32_e32 v150, v174

; #define LAS __attribute__((address_space(3)))
; #define LAS __attribute__((address_space(3)))
;     LAS unsigned* scr = (LAS unsigned*)(lds + wave * 16384);
;     WItem d0, d1; WRegs R0, R1;
;     constexpr int KB_ = DM / 32;
;     constexpr int NALL = EARLY ? KB_ * (INW / 128) : KB_ * (DM / 128) + KB_ * (CW / 128) + KB_ * (2 * CW / 128) + (CW / 32) * (DM / 128) + KB_ * (DFF2 / 128) + (DFF / 32) * (DM / 128);
;     const int hi_all = it_hi < NALL ? it_hi : NALL, total = hi_all - it_lo, nwgs = NGW / NWAVES, chunk = (((total + nwgs - 1) / nwgs) + NWAVES - 1) / NWAVES * NWAVES;
;     int it = it_lo + (gw / NWAVES) * chunk + (gw % NWAVES); const int wend0 = it_lo + (gw / NWAVES + 1) * chunk, wend = wend0 < hi_all ? wend0 : hi_all;
; __global__ void __launch_bounds__(NWAVES * 64, 2) mk_fwd(Args args) {
;     ...
;         { pg8::Gemm g{(const bf16*)(ws + WS_MB), (const bf16*)(ws + WS_WQKV) + (size_t)CW * DM, BATCH * NMEM, 2 * CW, DM, DM}; pg8::StaticOrder S; S.init(BATCH * NMEM, 2 * CW, G, (bx + G / 2) % G);
;           pg8::EpiScaleF32 E{(float*)(ws + WS_CKV), 2 * CW, (const float*)(ws + WS_SSQM)};
;           pg8::gemm_phase<pg8::EpiScaleF32, pg8::StaticOrder, true, true>(lds, g, S, E); }
;         if (CONV_OVERLAP && G >= 192 && bx >= G / 2 + 8) { __syncthreads(); convert_weights<false, true>(P, lds, (bx - (G / 2 + 8)) * NWAVES + wave, (G - (G / 2 + 8)) * NWAVES, wave, lane, LATE_SPLIT, 0x7fffffff); }
.LBB0_925:
	s_cmpk_lt_i32 s2, 0x88
	s_cbranch_scc1 .Lp6_hook_done
	s_cmp_lg_u32 s80, 0x100
	s_cbranch_scc1 .Lp6_hook_done
	s_cmp_gt_i32 s74, 4
	s_cbranch_scc1 .Lp6_hook_done
	s_cmp_lt_i32 s75, 7
	s_cbranch_scc1 .Lp6_hook_done
	v_writelane_b32 v255, s8, 8
	v_writelane_b32 v255, s9, 9
	v_writelane_b32 v255, s12, 10
	v_writelane_b32 v255, s16, 11
	v_writelane_b32 v255, s18, 12
	v_writelane_b32 v255, s19, 13
	v_writelane_b32 v255, s20, 14
	v_writelane_b32 v255, s21, 15
	v_writelane_b32 v255, s23, 16
	v_writelane_b32 v255, s24, 17
	v_writelane_b32 v255, s26, 18
	v_writelane_b32 v255, s34, 19
	v_readlane_b32 s70, v254, 0
	v_readlane_b32 s71, v254, 1
	v_and_b32_e32 v1, 63, v0
	v_readfirstlane_b32 s101, v0
	s_sub_u32 s100, s2, 0x88
	s_lshl_b32 s100, s100, 3
	s_sub_u32 s70, s70, 0xc0
	s_subb_u32 s71, s71, 0
	s_lshr_b32 s101, s101, 6
	s_add_u32 s101, s101, s100
	s_mov_b32 s100, 120
	s_mov_b32 s0, 0x3fc0
	v_writelane_b32 v255, s0, 2
	s_mov_b32 s0, 0x5940
	v_writelane_b32 v255, s0, 3
	s_mov_b32 s98, 1
	s_mov_b32 s99, 1
	s_mov_b64 s[4:5], -1
	s_branch .Lp4_conv_entry
